# gqa16 tile loop: one static priority raise (s_setprio 2) for waves 4-7, the second wave of each SIMD, restored to 1 behind the loop
# speedup vs baseline: 1.0028x; 1.0028x over previous
; #define HLOADV(kt) do { const char* vb_ = (const char*)Vh + (size_t)(kt) * (64 * LDK * 2); sv0 = *(const bf16x8*)(vb_ + koff0); sv1 = *(const bf16x8*)(vb_ + koff1); } while (0)
; #define HLOADK(kt) do { const char* kb_ = (const char*)Kh + (size_t)(kt) * (64 * LDK * 2); sk0 = *(const bf16x8*)(kb_ + koff0); sk1 = *(const bf16x8*)(kb_ + koff1); } while (0)
; #define HWRITEV(b) do { char* d_ = V_lds + (b) * G16_V; *(bf16x8*)(d_ + vst0) = sv0; *(bf16x8*)(d_ + vst1) = sv1; } while (0)
; #define HWRITEK(b) do { char* d_ = K_lds + (b) * GB_K; *(bf16x8*)(d_ + KSWZ(sr, sc * 2)) = sk0; *(bf16x8*)(d_ + KSWZ(32 + sr, sc * 2)) = sk1; } while (0)
; #define HEXP() do { _Pragma("unroll") for (int kt = 0; kt < 4; ++kt) { _Pragma("unroll") for (int qt = 0; qt < 2; ++qt) { _Pragma("unroll") for (int i = 0; i < 4; ++i) s[kt][qt][i] = __builtin_amdgcn_exp2f(fmaf(s[kt][qt][i], C, mnC)); } } } while (0)
; template <int LDQ, int LDK, int LDO>
; __device__ __forceinline__ void attn_gqa16_body(const bf16* __restrict__ Qb, const bf16* __restrict__ Kh, const bf16* __restrict__ Vh, bf16* __restrict__ Ob, int seq, char* lds, float mref) {
;     ...
;   { int l16q = l16, gq = g, widq = wid; asm volatile("" : "+v"(l16q), "+v"(gq), "+v"(widq));
;     const bf16* Qw = Qb + (widq >> 2) * 128 + (long)((widq & 3) * QBLK + l16q) * LDQ + gq * 8;
; #pragma unroll
;     for (int qt = 0; qt < 2; ++qt)
; #pragma unroll
;       for (int ds = 0; ds < 4; ++ds) qr[qt][ds] = *reinterpret_cast<const bf16x8*>(Qw + (long)qt * 16 * LDQ + ds * 32); }
;   const int sr = tid >> 4, sc = (tid & 15) * 8;
;   const int vst0 = (sc >> 4) * VP16 + sr * 32 + ((sc >> 3) & 1) * 16, vst1 = vst0 + 1024;
;   const int vb0 = (int)(uintptr_t)V_lds + (4 * g + (l16 >> 2)) * 32 + (l16 & 3) * 8;
;   const int kb0 = l16 * 272 + g * 16;
;   bf16x8 sv0, sv1, sk0, sk1;
;   const unsigned koff0 = (unsigned)(sr * LDK + sc) * 2u, koff1 = koff0 + 32u * LDK * 2u;
;     ...
;   f32x4a s[4][2]; bf16x8 pb[2][2];
;     ...
;   const int NT = seq / KVBLK;
;   HLOADK(0); HLOADV(0); asm volatile("s_waitcnt vmcnt(0)" ::: "memory"); HWRITEK(0); HWRITEV(0);
;   HLOADK(1); asm volatile("s_waitcnt vmcnt(0)" ::: "memory"); HWRITEK(1); __syncthreads();
;   HLOADK(2); HLOADV(1);
;   HQK(0); HEXP();
.LBB0_646:
	s_and_b64 vcc, exec, s[14:15]
	s_cbranch_vccz .LBB0_641
	s_lshl_b32 s8, s45, 7
	s_and_b32 s8, s8, 0x3f80
	s_ashr_i32 s14, s45, 8
	s_mul_i32 s12, s8, 0x2400
	s_add_u32 s15, s33, s12
	s_addc_u32 s17, s35, 0
	s_lshl_b32 s13, s45, 1
	s_lshl_b32 s12, s14, 9
	s_and_b32 s13, s13, 0x100
	s_or_b32 s12, s12, s13
	s_ashr_i32 s13, s12, 31
	v_mov_b32_e32 v4, v180
	v_mov_b32_e32 v2, v185
	v_mov_b32_e32 v5, v176
	s_lshl_b64 s[12:13], s[12:13], 1
	s_add_u32 s16, s15, s12
	v_lshlrev_b32_e32 v6, 5, v2
	v_and_b32_e32 v2, 0xffffff80, v6
	s_addc_u32 s17, s17, s13
	v_ashrrev_i32_e32 v3, 31, v2
	v_and_b32_e32 v6, 0x60, v6
	s_lshl_b32 s14, s14, 7
	v_lshl_add_u64 v[2:3], v[2:3], 1, s[16:17]
	v_add_u32_e32 v4, v6, v4
	s_ashr_i32 s15, s14, 31
	v_mad_i64_i32 v[2:3], s[16:17], v4, s26, v[2:3]
	v_lshlrev_b32_e32 v4, 3, v5
	s_lshl_b64 s[46:47], s[14:15], 1
	v_ashrrev_i32_e32 v5, 31, v4
	s_add_u32 s48, s21, s46
	v_lshl_add_u64 v[6:7], v[4:5], 1, v[2:3]
	s_addc_u32 s49, s22, s47
	global_load_dwordx4 v[30:33], v[6:7], off
	global_load_dwordx4 v[18:21], v[6:7], off offset:64
	global_load_dwordx4 v[10:13], v[6:7], off offset:128
	global_load_dwordx4 v[2:5], v[6:7], off offset:192
	v_add_co_u32_e32 v6, vcc, s27, v6
	s_add_u32 s46, s23, s46
	s_nop 0
	v_addc_co_u32_e32 v7, vcc, 0, v7, vcc
	v_lshl_add_u64 v[102:103], s[48:49], 0, v[178:179]
	s_addc_u32 s47, s24, s47
	s_add_u32 s74, s46, 0x90000
	s_addc_u32 s75, s47, 0
	s_add_u32 s76, s74, 0x48000
	s_addc_u32 s77, s75, 0
	v_add_co_u32_e32 v34, vcc, s28, v102
	v_lshl_add_u64 v[104:105], s[46:47], 0, v[178:179]
	s_nop 0
	v_addc_co_u32_e32 v35, vcc, 0, v103, vcc
	v_add_co_u32_e32 v46, vcc, s28, v104
	global_load_dwordx4 v[38:41], v[6:7], off
	global_load_dwordx4 v[22:25], v[6:7], off offset:64
	global_load_dwordx4 v[14:17], v[6:7], off offset:128
	s_nop 0
	global_load_dwordx4 v[6:9], v[6:7], off offset:192
	v_addc_co_u32_e32 v47, vcc, 0, v105, vcc
	v_add_co_u32_e32 v50, vcc, s29, v102
	global_load_dwordx4 v[26:29], v[102:103], off
	s_nop 0
	global_load_dwordx4 v[34:37], v[34:35], off
	v_addc_co_u32_e32 v51, vcc, 0, v103, vcc
	v_add_co_u32_e32 v54, vcc, s30, v102
	global_load_dwordx4 v[42:45], v[104:105], off
	s_nop 0
	global_load_dwordx4 v[46:49], v[46:47], off
	s_waitcnt vmcnt(0)
	v_addc_co_u32_e32 v55, vcc, 0, v103, vcc
	global_load_dwordx4 v[50:53], v[50:51], off
	s_nop 0
	global_load_dwordx4 v[54:57], v[54:55], off
	s_waitcnt vmcnt(5)
	ds_write_b128 v194, v[26:29] offset:33280
	s_waitcnt vmcnt(4)
	ds_write_b128 v194, v[34:37] offset:41984
	s_waitcnt vmcnt(3)
	ds_write_b128 v181, v[42:45]
	s_waitcnt vmcnt(2)
	ds_write_b128 v181, v[46:49] offset:1024
	s_waitcnt vmcnt(0)
	s_waitcnt vmcnt(1)
	ds_write_b128 v194, v[50:53] offset:50688
	s_waitcnt vmcnt(0)
	ds_write_b128 v194, v[54:57] offset:59392
	s_waitcnt lgkmcnt(0)
	s_barrier
	ds_read_b128 v[26:29], v182 offset:33280
	ds_read_b128 v[34:37], v182 offset:33344
	ds_read_b128 v[46:49], v182 offset:37632
	ds_read_b128 v[50:53], v182 offset:37696
	ds_read_b128 v[58:61], v182 offset:41984
	ds_read_b128 v[62:65], v182 offset:42048
	ds_read_b128 v[70:73], v182 offset:46336
	ds_read_b128 v[74:77], v182 offset:46400
	s_waitcnt lgkmcnt(7)
	v_mfma_f32_16x16x32_bf16 v[42:45], v[26:29], v[30:33], 0
	v_mfma_f32_16x16x32_bf16 v[26:29], v[26:29], v[38:41], 0
	s_waitcnt lgkmcnt(5)
	v_mfma_f32_16x16x32_bf16 v[54:57], v[46:49], v[30:33], 0
	v_mfma_f32_16x16x32_bf16 v[46:49], v[46:49], v[38:41], 0
	s_waitcnt lgkmcnt(3)
	v_mfma_f32_16x16x32_bf16 v[66:69], v[58:61], v[30:33], 0
	v_mfma_f32_16x16x32_bf16 v[58:61], v[58:61], v[38:41], 0
	s_waitcnt lgkmcnt(1)
	v_mfma_f32_16x16x32_bf16 v[78:81], v[70:73], v[30:33], 0
	v_mfma_f32_16x16x32_bf16 v[70:73], v[70:73], v[38:41], 0
	v_mfma_f32_16x16x32_bf16 v[42:45], v[34:37], v[18:21], v[42:45]
	v_mfma_f32_16x16x32_bf16 v[26:29], v[34:37], v[22:25], v[26:29]
	v_mfma_f32_16x16x32_bf16 v[34:37], v[50:53], v[18:21], v[54:57]
	v_mfma_f32_16x16x32_bf16 v[46:49], v[50:53], v[22:25], v[46:49]
	v_mfma_f32_16x16x32_bf16 v[50:53], v[62:65], v[18:21], v[66:69]
	v_mfma_f32_16x16x32_bf16 v[54:57], v[62:65], v[22:25], v[58:61]
	s_waitcnt lgkmcnt(0)
	v_mfma_f32_16x16x32_bf16 v[58:61], v[74:77], v[18:21], v[78:81]
	v_mfma_f32_16x16x32_bf16 v[62:65], v[74:77], v[22:25], v[70:73]
	ds_read_b128 v[66:69], v182 offset:33408
	ds_read_b128 v[74:77], v182 offset:33472
	s_waitcnt lgkmcnt(1)
	v_mfma_f32_16x16x32_bf16 v[42:45], v[66:69], v[10:13], v[42:45]
	v_mfma_f32_16x16x32_bf16 v[26:29], v[66:69], v[14:17], v[26:29]
	ds_read_b128 v[66:69], v182 offset:37760
	ds_read_b128 v[78:81], v182 offset:37824
	s_waitcnt lgkmcnt(1)
	v_mfma_f32_16x16x32_bf16 v[34:37], v[66:69], v[10:13], v[34:37]
	v_mfma_f32_16x16x32_bf16 v[46:49], v[66:69], v[14:17], v[46:49]
	ds_read_b128 v[66:69], v182 offset:42112
	ds_read_b128 v[82:85], v182 offset:42176
	s_waitcnt lgkmcnt(1)
	v_mfma_f32_16x16x32_bf16 v[50:53], v[66:69], v[10:13], v[50:53]
	v_mfma_f32_16x16x32_bf16 v[86:89], v[66:69], v[14:17], v[54:57]
	s_nop 2
	ds_read_b128 v[54:57], v182 offset:46464
	ds_read_b128 v[90:93], v182 offset:46528
	v_mfma_f32_16x16x32_bf16 v[66:69], v[74:77], v[6:9], v[26:29]
	s_nop 2
	v_add_co_u32_e32 v26, vcc, s25, v102
	s_waitcnt lgkmcnt(1)
	v_mfma_f32_16x16x32_bf16 v[98:101], v[54:57], v[14:17], v[62:65]
	v_addc_co_u32_e32 v27, vcc, 0, v103, vcc
	v_add_co_u32_e32 v28, vcc, s31, v102
	v_mfma_f32_16x16x32_bf16 v[62:65], v[78:81], v[2:5], v[34:37]
	s_nop 0
	v_addc_co_u32_e32 v29, vcc, 0, v103, vcc
	global_load_dwordx4 v[106:109], v[26:27], off
	global_load_dwordx4 v[110:113], v[28:29], off
	v_add_co_u32_e32 v26, vcc, s29, v104
	v_mfma_f32_16x16x32_bf16 v[94:97], v[54:57], v[10:13], v[58:61]
	s_nop 0
	v_addc_co_u32_e32 v27, vcc, 0, v105, vcc
	v_add_co_u32_e32 v34, vcc, s30, v104
	v_mfma_f32_16x16x32_bf16 v[70:73], v[74:77], v[2:5], v[42:45]
	s_nop 0
	v_addc_co_u32_e32 v35, vcc, 0, v105, vcc
	s_nop 0
	v_mfma_f32_16x16x32_bf16 v[58:61], v[78:81], v[6:9], v[46:49]
	v_mfma_f32_16x16x32_bf16 v[54:57], v[82:85], v[2:5], v[50:53]
	v_mfma_f32_16x16x32_bf16 v[50:53], v[82:85], v[6:9], v[86:89]
	s_waitcnt lgkmcnt(0)
; #define HLOADV(kt) do { const char* vb_ = (const char*)Vh + (size_t)(kt) * (64 * LDK * 2); sv0 = *(const bf16x8*)(vb_ + koff0); sv1 = *(const bf16x8*)(vb_ + koff1); } while (0)
; #define HLOADK(kt) do { const char* kb_ = (const char*)Kh + (size_t)(kt) * (64 * LDK * 2); sk0 = *(const bf16x8*)(kb_ + koff0); sk1 = *(const bf16x8*)(kb_ + koff1); } while (0)
; #define HWRITEV(b) do { char* d_ = V_lds + (b) * G16_V; *(bf16x8*)(d_ + vst0) = sv0; *(bf16x8*)(d_ + vst1) = sv1; } while (0)
; #define HWRITEK(b) do { char* d_ = K_lds + (b) * GB_K; *(bf16x8*)(d_ + KSWZ(sr, sc * 2)) = sk0; *(bf16x8*)(d_ + KSWZ(32 + sr, sc * 2)) = sk1; } while (0)
; #define HEXP() do { _Pragma("unroll") for (int kt = 0; kt < 4; ++kt) { _Pragma("unroll") for (int qt = 0; qt < 2; ++qt) { _Pragma("unroll") for (int i = 0; i < 4; ++i) s[kt][qt][i] = __builtin_amdgcn_exp2f(fmaf(s[kt][qt][i], C, mnC)); } } } while (0)
; template <int LDQ, int LDK, int LDO>
; __device__ __forceinline__ void attn_gqa16_body(const bf16* __restrict__ Qb, const bf16* __restrict__ Kh, const bf16* __restrict__ Vh, bf16* __restrict__ Ob, int seq, char* lds, float mref) {
;     ...
;   const int NT = seq / KVBLK;
;   HLOADK(0); HLOADV(0); asm volatile("s_waitcnt vmcnt(0)" ::: "memory"); HWRITEK(0); HWRITEV(0);
;   HLOADK(1); asm volatile("s_waitcnt vmcnt(0)" ::: "memory"); HWRITEK(1); __syncthreads();
;   HLOADK(2); HLOADV(1);
;   HQK(0); HEXP();
;   if (wid >= 4) __builtin_amdgcn_s_setprio(1);
;   for (int t = 0; t < NT; ++t) {
;     HPACK();
;     __syncthreads();
	v_mfma_f32_16x16x32_bf16 v[46:49], v[90:93], v[2:5], v[94:97]
	v_mfma_f32_16x16x32_bf16 v[42:45], v[90:93], v[6:9], v[98:101]
	s_and_saveexec_b64 s[16:17], s[4:5]
	s_setprio 1
	s_or_b64 exec, exec, s[16:17]
	v_add_f32_e32 v70, v186, v70
	v_add_f32_e32 v66, v186, v66
	v_add_f32_e32 v62, v186, v62
	v_add_f32_e32 v58, v186, v58
	v_add_f32_e32 v54, v186, v54
	v_add_f32_e32 v50, v186, v50
	v_add_f32_e32 v46, v186, v46
	v_add_f32_e32 v42, v186, v42
	v_exp_f32_e32 v158, v70
	v_add_f32_e32 v70, v186, v71
	v_exp_f32_e32 v159, v66
	v_add_f32_e32 v66, v186, v67
	v_exp_f32_e32 v168, v62
	v_add_f32_e32 v62, v186, v63
	v_exp_f32_e32 v169, v58
	v_add_f32_e32 v58, v186, v59
	v_exp_f32_e32 v142, v54
	v_add_f32_e32 v54, v186, v55
	v_exp_f32_e32 v143, v50
	v_add_f32_e32 v50, v186, v51
	v_exp_f32_e32 v134, v46
	v_add_f32_e32 v46, v186, v47
	v_exp_f32_e32 v135, v42
	v_add_f32_e32 v42, v186, v43
	v_exp_f32_e32 v152, v70
	v_add_f32_e32 v70, v186, v72
	v_exp_f32_e32 v153, v66
	v_add_f32_e32 v66, v186, v68
	v_exp_f32_e32 v170, v62
	v_add_f32_e32 v62, v186, v64
	v_exp_f32_e32 v171, v58
	v_add_f32_e32 v58, v186, v60
	v_exp_f32_e32 v172, v54
	v_add_f32_e32 v54, v186, v56
	v_exp_f32_e32 v173, v50
	v_add_f32_e32 v50, v186, v52
	v_exp_f32_e32 v138, v46
	v_add_f32_e32 v46, v186, v48
	v_exp_f32_e32 v139, v42
	v_add_f32_e32 v42, v186, v44
	v_exp_f32_e32 v156, v70
	v_add_f32_e32 v70, v186, v73
	v_exp_f32_e32 v157, v66
	v_add_f32_e32 v66, v186, v69
	v_exp_f32_e32 v164, v62
	v_add_f32_e32 v62, v186, v65
	v_exp_f32_e32 v165, v58
	v_add_f32_e32 v58, v186, v61
	v_exp_f32_e32 v144, v54
	v_add_f32_e32 v54, v186, v57
	v_exp_f32_e32 v145, v50
	v_add_f32_e32 v50, v186, v53
	v_exp_f32_e32 v136, v46
	v_add_f32_e32 v46, v186, v49
	v_exp_f32_e32 v137, v42
	v_add_f32_e32 v42, v186, v45
	v_exp_f32_e32 v160, v70
	v_exp_f32_e32 v161, v66
	v_exp_f32_e32 v166, v62
	v_exp_f32_e32 v167, v58
	v_exp_f32_e32 v174, v54
	v_exp_f32_e32 v175, v50
	v_exp_f32_e32 v140, v46
	v_exp_f32_e32 v141, v42
	v_mov_b32_e32 v50, 0
	v_lshl_add_u64 v[162:163], s[14:15], 1, v[154:155]
	s_mov_b32 s16, 0
	s_mov_b64 s[14:15], 0
	v_mov_b32_e32 v51, v50
	v_mov_b32_e32 v52, v50
	v_mov_b32_e32 v53, v50
	v_mov_b32_e32 v78, v50
	v_mov_b32_e32 v79, v50
	v_mov_b32_e32 v80, v50
	v_mov_b32_e32 v81, v50
	v_mov_b32_e32 v90, v50
	v_mov_b32_e32 v91, v50
	v_mov_b32_e32 v92, v50
	v_mov_b32_e32 v93, v50
	v_mov_b32_e32 v94, v50
	v_mov_b32_e32 v95, v50
	v_mov_b32_e32 v96, v50
	v_mov_b32_e32 v97, v50
	v_mov_b32_e32 v98, v50
	v_mov_b32_e32 v99, v50
	v_mov_b32_e32 v100, v50
	v_mov_b32_e32 v101, v50
	v_mov_b32_e32 v102, v50
	v_mov_b32_e32 v103, v50
	v_mov_b32_e32 v104, v50
	v_mov_b32_e32 v105, v50
	v_mov_b32_e32 v82, v50
	v_mov_b32_e32 v83, v50
	v_mov_b32_e32 v84, v50
	v_mov_b32_e32 v85, v50
	v_mov_b32_e32 v86, v50
	v_mov_b32_e32 v87, v50
	v_mov_b32_e32 v88, v50
	v_mov_b32_e32 v89, v50
	v_mov_b32_e32 v54, v50
	v_mov_b32_e32 v55, v50
	v_mov_b32_e32 v56, v50
	v_mov_b32_e32 v57, v50
	v_mov_b32_e32 v62, v50
	v_mov_b32_e32 v63, v50
	v_mov_b32_e32 v64, v50
	v_mov_b32_e32 v65, v50
	v_mov_b32_e32 v58, v50
	v_mov_b32_e32 v59, v50
	v_mov_b32_e32 v60, v50
	v_mov_b32_e32 v61, v50
	v_mov_b32_e32 v70, v50
	v_mov_b32_e32 v71, v50
	v_mov_b32_e32 v72, v50
	v_mov_b32_e32 v73, v50
	v_mov_b32_e32 v42, v50
	v_mov_b32_e32 v43, v50
	v_mov_b32_e32 v44, v50
	v_mov_b32_e32 v45, v50
	v_mov_b32_e32 v46, v50
	v_mov_b32_e32 v47, v50
	v_mov_b32_e32 v48, v50
	v_mov_b32_e32 v49, v50
	v_mov_b32_e32 v66, v50
	v_mov_b32_e32 v67, v50
	v_mov_b32_e32 v68, v50
	v_mov_b32_e32 v69, v50
	v_mov_b32_e32 v74, v50
	v_mov_b32_e32 v75, v50
	v_mov_b32_e32 v76, v50
	v_mov_b32_e32 v77, v50
	v_mov_b32_e32 v150, v50
	v_mov_b32_e32 v151, v50
	s_cmp_ge_u32 s84, 0x2080
	s_cbranch_scc0 .Lvg_prio
	s_setprio 2
.Lvg_prio:
	v_mov_b32_e32 v240, v156
	v_mov_b32_e32 v241, v157
	v_mov_b32_e32 v246, v158
	v_mov_b32_e32 v247, v159
	v_mov_b32_e32 v242, v164
	v_mov_b32_e32 v243, v165
	v_mov_b32_e32 v244, v166
	v_mov_b32_e32 v245, v167
	s_nop 0
	s_nop 0
	s_nop 0
.LBB0_650:
	s_add_i32 s17, s16, 1
	s_and_b32 s16, s16, 1
	s_and_b32 s46, 1, s17
	s_cmp_eq_u32 s46, 1
	s_cselect_b32 s85, s86, s84
	s_cselect_b32 s46, 0x4400, 0
	v_add_u32_e32 v189, s46, v182
	v_cvt_pk_bf16_f32 v124, v134, v138
	v_cvt_pk_bf16_f32 v125, v136, v140
	v_cvt_pk_bf16_f32 v128, v135, v139
	v_cvt_pk_bf16_f32 v129, v137, v141
	s_waitcnt vmcnt(2)
	s_barrier
; #define SBAR() __builtin_amdgcn_sched_barrier(0)
; template <int LDQ, int LDK, int LDO>
; __device__ __forceinline__ void attn_gqa16_body(const bf16* __restrict__ Qb, const bf16* __restrict__ Kh, const bf16* __restrict__ Vh, bf16* __restrict__ Ob, int seq, char* lds, float mref) {
;     ...
;     HPACK();
;     __syncthreads();
;     const bool more = t + 1 < NT;
;     if (more) HQK((t + 1) & 1);
;     const int vb = vb0 + (t & 1) * (int)G16_V;
;     SBAR(); pv16<0>(o, vb, pb); SBAR();
	ds_read_b128 v[130:133], v189 offset:33280
	ds_read_b128 v[146:149], v189 offset:33344
	ds_read_b128 v[200:203], v189 offset:37632
	ds_read_b128 v[204:207], v189 offset:37696
	ds_read_b128 v[212:215], v189 offset:41984
	ds_read_b128 v[216:219], v189 offset:42048
	ds_read_b128 v[224:227], v189 offset:46336
	ds_read_b128 v[228:231], v189 offset:46400
	s_mov_b32 m0, s85
	s_nop 0
	global_load_lds_dwordx4 v253, s[74:75]
	s_add_i32 m0, s85, 0x400
	s_nop 0
	global_load_lds_dwordx4 v253, s[76:77]
	s_add_u32 s74, s74, 0x90000
	s_addc_u32 s75, s75, 0
	s_add_u32 s76, s76, 0x90000
	s_addc_u32 s77, s77, 0
	s_waitcnt lgkmcnt(7)
	v_mfma_f32_16x16x32_bf16 v[196:199], v[130:133], v[30:33], v[248:251]
	v_add_f32_e64 v134, v134, v138
	v_add_f32_e64 v135, v135, v139
	v_pk_add_f32 v[136:137], v[136:137], v[140:141]
	s_mul_i32 s46, s16, 0x4100
	v_mfma_f32_16x16x32_bf16 v[130:133], v[130:133], v[38:41], v[248:251]
	v_cvt_pk_bf16_f32 v114, v246, v152
	s_waitcnt lgkmcnt(5)
	v_mfma_f32_16x16x32_bf16 v[208:211], v[200:203], v[30:33], v[248:251]
	v_cvt_pk_bf16_f32 v115, v240, v160
	v_mfma_f32_16x16x32_bf16 v[200:203], v[200:203], v[38:41], v[248:251]
	v_cvt_pk_bf16_f32 v116, v168, v170
	s_waitcnt lgkmcnt(3)
	v_mfma_f32_16x16x32_bf16 v[220:223], v[212:215], v[30:33], v[248:251]
	v_cvt_pk_bf16_f32 v117, v242, v244
	v_mfma_f32_16x16x32_bf16 v[212:215], v[212:215], v[38:41], v[248:251]
	v_cvt_pk_bf16_f32 v118, v247, v153
	s_waitcnt lgkmcnt(1)
	v_mfma_f32_16x16x32_bf16 v[232:235], v[224:227], v[30:33], v[248:251]
	v_cvt_pk_bf16_f32 v119, v241, v161
	v_mfma_f32_16x16x32_bf16 v[224:227], v[224:227], v[38:41], v[248:251]
	v_cvt_pk_bf16_f32 v120, v169, v171
	v_mfma_f32_16x16x32_bf16 v[196:199], v[146:149], v[18:21], v[196:199]
	v_cvt_pk_bf16_f32 v121, v243, v245
	v_mfma_f32_16x16x32_bf16 v[130:133], v[146:149], v[22:25], v[130:133]
	v_cvt_pk_bf16_f32 v122, v142, v172
	v_mfma_f32_16x16x32_bf16 v[146:149], v[204:207], v[18:21], v[208:211]
	v_cvt_pk_bf16_f32 v123, v144, v174
	v_mfma_f32_16x16x32_bf16 v[200:203], v[204:207], v[22:25], v[200:203]
	v_cvt_pk_bf16_f32 v126, v143, v173
	v_mfma_f32_16x16x32_bf16 v[204:207], v[216:219], v[18:21], v[220:223]
	v_cvt_pk_bf16_f32 v127, v145, v175
	v_mfma_f32_16x16x32_bf16 v[208:211], v[216:219], v[22:25], v[212:215]
	s_waitcnt lgkmcnt(0)
	v_mfma_f32_16x16x32_bf16 v[216:219], v[228:231], v[22:25], v[224:227]
	ds_read_b128 v[220:223], v189 offset:33408
	s_nop 1
	ds_read_b128 v[224:227], v189 offset:33472
	v_mfma_f32_16x16x32_bf16 v[212:215], v[228:231], v[18:21], v[232:235]
	s_waitcnt lgkmcnt(1)
	v_mfma_f32_16x16x32_bf16 v[196:199], v[220:223], v[10:13], v[196:199]
	v_mfma_f32_16x16x32_bf16 v[130:133], v[220:223], v[14:17], v[130:133]
	ds_read_b128 v[220:223], v189 offset:37760
	ds_read_b128 v[228:231], v189 offset:37824
	s_waitcnt lgkmcnt(1)
	v_mfma_f32_16x16x32_bf16 v[146:149], v[220:223], v[10:13], v[146:149]
	v_mfma_f32_16x16x32_bf16 v[200:203], v[220:223], v[14:17], v[200:203]
	ds_read_b128 v[220:223], v189 offset:42112
	ds_read_b128 v[232:235], v189 offset:42176
	s_waitcnt lgkmcnt(1)
	v_mfma_f32_16x16x32_bf16 v[204:207], v[220:223], v[10:13], v[204:207]
	v_mfma_f32_16x16x32_bf16 v[208:211], v[220:223], v[14:17], v[208:211]
	ds_read_b128 v[220:223], v189 offset:46464
	ds_read_b128 v[236:239], v189 offset:46528
	v_add_u32_e32 v189, s46, v183
	s_waitcnt lgkmcnt(1)
	v_mfma_f32_16x16x32_bf16 v[212:215], v[220:223], v[10:13], v[212:215]
	v_mfma_f32_16x16x32_bf16 v[216:219], v[220:223], v[14:17], v[216:219]
	v_mfma_f32_16x16x32_bf16 v[220:223], v[224:227], v[6:9], v[130:133]
	s_nop 2
	v_add_f32_e64 v130, v246, v152
	v_add_f32_e64 v131, v247, v153
	v_pk_add_f32 v[132:133], v[240:241], v[160:161]
	v_pk_add_f32 v[152:153], v[168:169], v[170:171]
	v_pk_add_f32 v[156:157], v[242:243], v[244:245]
	v_pk_add_f32 v[158:159], v[142:143], v[172:173]
	v_pk_add_f32 v[160:161], v[144:145], v[174:175]
	v_pk_add_f32 v[130:131], v[130:131], v[132:133]
	v_mfma_f32_16x16x32_bf16 v[142:145], v[232:235], v[2:5], v[204:207]
	v_add_f32_e64 v152, v152, v156
	v_add_f32_e64 v153, v153, v157
	v_pk_add_f32 v[156:157], v[158:159], v[160:161]
	v_pk_add_f32 v[158:159], v[134:135], v[136:137]
	v_mfma_f32_16x16x32_bf16 v[138:141], v[232:235], v[6:9], v[208:211]
	v_add_f32_e64 v150, v150, v130
	v_add_f32_e64 v151, v151, v131
	v_pk_add_f32 v[150:151], v[152:153], v[150:151]
	s_waitcnt lgkmcnt(0)
	v_mfma_f32_16x16x32_bf16 v[134:137], v[236:239], v[2:5], v[212:215]
	v_add_f32_e64 v150, v156, v150
	v_add_f32_e64 v151, v157, v151
	v_pk_add_f32 v[150:151], v[158:159], v[150:151]
	v_mfma_f32_16x16x32_bf16 v[196:199], v[224:227], v[2:5], v[196:199]
	v_mfma_f32_16x16x32_bf16 v[224:227], v[228:231], v[2:5], v[146:149]
	v_mfma_f32_16x16x32_bf16 v[146:149], v[228:231], v[6:9], v[200:203]
	v_mfma_f32_16x16x32_bf16 v[130:133], v[236:239], v[6:9], v[216:219]
	ds_read_b64_tr_b16 v[156:157], v189 offset:0
	ds_read_b64_tr_b16 v[158:159], v189 offset:0x200
	ds_read_b64_tr_b16 v[164:165], v189 offset:0x400
	ds_read_b64_tr_b16 v[166:167], v189 offset:0x600
	ds_read_b64_tr_b16 v[168:169], v189 offset:0x820
	ds_read_b64_tr_b16 v[170:171], v189 offset:0xa20
	ds_read_b64_tr_b16 v[172:173], v189 offset:0xc20
	ds_read_b64_tr_b16 v[174:175], v189 offset:0xe20
	ds_read_b64_tr_b16 v[200:201], v189 offset:0x1040
	ds_read_b64_tr_b16 v[202:203], v189 offset:0x1240
	ds_read_b64_tr_b16 v[204:205], v189 offset:0x1440
	ds_read_b64_tr_b16 v[206:207], v189 offset:0x1640
	s_waitcnt lgkmcnt(4)
; #define SBAR() __builtin_amdgcn_sched_barrier(0)
; #define MFMA16(a, b, c) __builtin_amdgcn_mfma_f32_16x16x32_bf16(a, b, c, 0, 0, 0)
; template <int D0> __device__ __forceinline__ void pv16(f32x4a (&o)[8][2], int vb, const bf16x8 (&pb)[2][2]) {
;     ...
;   const s16x4 a0 = TR(D0, 0, 0), a1 = TR(D0, 0, 1), a2 = TR(D0, 1, 0), a3 = TR(D0, 1, 1), b0 = TR(D0 + 1, 0, 0), b1 = TR(D0 + 1, 0, 1), b2 = TR(D0 + 1, 1, 0), b3 = TR(D0 + 1, 1, 1);
;   const s16x4 c0 = TR(D0 + 2, 0, 0), c1 = TR(D0 + 2, 0, 1), c2 = TR(D0 + 2, 1, 0), c3 = TR(D0 + 2, 1, 1);
;   asm volatile("s_waitcnt lgkmcnt(4)" ::: "memory"); SBAR();
;   o[D0][0] = MFMA16(PK16(a0, a1), pb[0][0], o[D0][0]); o[D0][1] = MFMA16(PK16(a0, a1), pb[0][1], o[D0][1]);
;   o[D0 + 1][0] = MFMA16(PK16(b0, b1), pb[0][0], o[D0 + 1][0]); o[D0 + 1][1] = MFMA16(PK16(b0, b1), pb[0][1], o[D0 + 1][1]);
;   o[D0][0] = MFMA16(PK16(a2, a3), pb[1][0], o[D0][0]); o[D0][1] = MFMA16(PK16(a2, a3), pb[1][1], o[D0][1]);
;   o[D0 + 1][0] = MFMA16(PK16(b2, b3), pb[1][0], o[D0 + 1][0]); o[D0 + 1][1] = MFMA16(PK16(b2, b3), pb[1][1], o[D0 + 1][1]);
;   SBAR();
;   const s16x4 d0 = TR(D0 + 3, 0, 0), d1 = TR(D0 + 3, 0, 1), d2 = TR(D0 + 3, 1, 0), d3 = TR(D0 + 3, 1, 1);
;   asm volatile("s_waitcnt lgkmcnt(4)" ::: "memory"); SBAR();
;   o[D0 + 2][0] = MFMA16(PK16(c0, c1), pb[0][0], o[D0 + 2][0]); o[D0 + 2][1] = MFMA16(PK16(c0, c1), pb[0][1], o[D0 + 2][1]);
;   o[D0 + 2][0] = MFMA16(PK16(c2, c3), pb[1][0], o[D0 + 2][0]); o[D0 + 2][1] = MFMA16(PK16(c2, c3), pb[1][1], o[D0 + 2][1]);
;   asm volatile("s_waitcnt lgkmcnt(0)" ::: "memory"); SBAR();
;   o[D0 + 3][0] = MFMA16(PK16(d0, d1), pb[0][0], o[D0 + 3][0]); o[D0 + 3][1] = MFMA16(PK16(d0, d1), pb[0][1], o[D0 + 3][1]);
;   o[D0 + 3][0] = MFMA16(PK16(d2, d3), pb[1][0], o[D0 + 3][0]); o[D0 + 3][1] = MFMA16(PK16(d2, d3), pb[1][1], o[D0 + 3][1]);
;     ...
; }
; template <int LDQ, int LDK, int LDO>
; __device__ __forceinline__ void attn_gqa16_body(const bf16* __restrict__ Qb, const bf16* __restrict__ Kh, const bf16* __restrict__ Vh, bf16* __restrict__ Ob, int seq, char* lds, float mref) {
;     ...
;     asm volatile("s_waitcnt vmcnt(0)" ::: "memory");
;     if (t + 2 < NT) HWRITEK(t & 1);
;     if (t + 1 < NT) HWRITEV((t + 1) & 1);
;     HLOADK(t + 3); HLOADV(t + 2);
;     SBAR(); pv16<4>(o, vb, pb); SBAR();
;     if (more) HEXP();
;   }
;   __builtin_amdgcn_s_setprio(0);
	s_nop 0
	v_mfma_f32_16x16x32_bf16 v[102:105], v[156:159], v[114:117], v[102:105]
	v_mfma_f32_16x16x32_bf16 v[98:101], v[156:159], v[118:121], v[98:101]
	v_mfma_f32_16x16x32_bf16 v[94:97], v[168:171], v[114:117], v[94:97]
	v_exp_f32_e32 v246, v196
	v_mfma_f32_16x16x32_bf16 v[90:93], v[168:171], v[118:121], v[90:93]
	v_exp_f32_e32 v240, v198
	v_mfma_f32_16x16x32_bf16 v[102:105], v[164:167], v[122:125], v[102:105]
	v_exp_f32_e32 v160, v199
	v_mfma_f32_16x16x32_bf16 v[98:101], v[164:167], v[126:129], v[98:101]
	v_exp_f32_e32 v247, v220
	v_mfma_f32_16x16x32_bf16 v[94:97], v[172:175], v[122:125], v[94:97]
	v_exp_f32_e32 v241, v222
	v_mfma_f32_16x16x32_bf16 v[90:93], v[172:175], v[126:129], v[90:93]
	v_exp_f32_e32 v161, v223
	ds_read_b64_tr_b16 v[156:157], v189 offset:0x1860
	ds_read_b64_tr_b16 v[158:159], v189 offset:0x1a60
	ds_read_b64_tr_b16 v[164:165], v189 offset:0x1c60
	ds_read_b64_tr_b16 v[166:167], v189 offset:0x1e60
	s_waitcnt lgkmcnt(4)
	v_mfma_f32_16x16x32_bf16 v[78:81], v[200:203], v[114:117], v[78:81]
	v_exp_f32_e32 v172, v143
	s_waitcnt lgkmcnt(0)
	v_mfma_f32_16x16x32_bf16 v[50:53], v[200:203], v[118:121], v[50:53]
	v_exp_f32_e32 v174, v145
	v_mfma_f32_16x16x32_bf16 v[78:81], v[204:207], v[122:125], v[78:81]
	v_exp_f32_e32 v143, v138
	v_mfma_f32_16x16x32_bf16 v[50:53], v[204:207], v[126:129], v[50:53]
	v_exp_f32_e32 v173, v139
	v_mfma_f32_16x16x32_bf16 v[82:85], v[156:159], v[114:117], v[82:85]
	v_exp_f32_e32 v145, v140
	v_mfma_f32_16x16x32_bf16 v[86:89], v[156:159], v[118:121], v[86:89]
	v_exp_f32_e32 v175, v141
	v_mfma_f32_16x16x32_bf16 v[82:85], v[164:167], v[122:125], v[82:85]
	v_exp_f32_e32 v138, v135
	v_mfma_f32_16x16x32_bf16 v[86:89], v[164:167], v[126:129], v[86:89]
	v_exp_f32_e32 v140, v137
	v_lshl_add_u64 v[152:153], v[162:163], 0, s[14:15]
	v_add_co_u32_e32 v156, vcc, s37, v152
	s_mulk_i32 s16, 0x4400
	s_nop 0
	v_addc_co_u32_e32 v157, vcc, 0, v153, vcc
	v_add_co_u32_e32 v158, vcc, s38, v152
	v_add_u32_e32 v164, s16, v194
	s_nop 0
	v_addc_co_u32_e32 v159, vcc, 0, v153, vcc
	s_waitcnt vmcnt(2)
	ds_write_b128 v164, v[106:109] offset:33280
	ds_write_b128 v164, v[110:113] offset:41984
	global_load_dwordx4 v[106:109], v[156:157], off offset:3072
	global_load_dwordx4 v[110:113], v[158:159], off offset:3072
	ds_read_b64_tr_b16 v[156:157], v189 offset:0x2080
	ds_read_b64_tr_b16 v[158:159], v189 offset:0x2280
	ds_read_b64_tr_b16 v[164:165], v189 offset:0x2480
	ds_read_b64_tr_b16 v[166:167], v189 offset:0x2680
	ds_read_b64_tr_b16 v[200:201], v189 offset:0x28a0
	ds_read_b64_tr_b16 v[202:203], v189 offset:0x2aa0
	ds_read_b64_tr_b16 v[204:205], v189 offset:0x2ca0
	ds_read_b64_tr_b16 v[206:207], v189 offset:0x2ea0
	s_waitcnt lgkmcnt(6)
	s_nop 0
	v_mfma_f32_16x16x32_bf16 v[54:57], v[156:159], v[114:117], v[54:57]
	v_exp_f32_e32 v135, v130
	v_mfma_f32_16x16x32_bf16 v[62:65], v[156:159], v[118:121], v[62:65]
	v_exp_f32_e32 v139, v131
	ds_read_b64_tr_b16 v[156:157], v189 offset:0x30c0
	ds_read_b64_tr_b16 v[158:159], v189 offset:0x32c0
	s_waitcnt lgkmcnt(4)
	v_mfma_f32_16x16x32_bf16 v[58:61], v[200:203], v[114:117], v[58:61]
	v_exp_f32_e32 v137, v132
	v_mfma_f32_16x16x32_bf16 v[70:73], v[200:203], v[118:121], v[70:73]
	v_exp_f32_e32 v141, v133
	ds_read_b64_tr_b16 v[200:201], v189 offset:0x38e0
	ds_read_b64_tr_b16 v[202:203], v189 offset:0x3ae0
	s_waitcnt lgkmcnt(6)
	v_mfma_f32_16x16x32_bf16 v[54:57], v[164:167], v[122:125], v[54:57]
	v_exp_f32_e32 v168, v224
	v_mfma_f32_16x16x32_bf16 v[62:65], v[164:167], v[126:129], v[62:65]
	v_exp_f32_e32 v170, v225
	ds_read_b64_tr_b16 v[164:165], v189 offset:0x34c0
	ds_read_b64_tr_b16 v[166:167], v189 offset:0x36c0
	s_waitcnt lgkmcnt(6)
	v_mfma_f32_16x16x32_bf16 v[58:61], v[204:207], v[122:125], v[58:61]
	v_exp_f32_e32 v169, v146
	v_mfma_f32_16x16x32_bf16 v[70:73], v[204:207], v[126:129], v[70:73]
	v_exp_f32_e32 v171, v147
	ds_read_b64_tr_b16 v[204:205], v189 offset:0x3ce0
	ds_read_b64_tr_b16 v[206:207], v189 offset:0x3ee0
	s_waitcnt lgkmcnt(6)
	v_mfma_f32_16x16x32_bf16 v[42:45], v[156:159], v[114:117], v[42:45]
	v_exp_f32_e32 v152, v197
	v_exp_f32_e32 v134, v134
	v_mfma_f32_16x16x32_bf16 v[46:49], v[156:159], v[118:121], v[46:49]
	v_exp_f32_e32 v153, v221
	v_exp_f32_e32 v136, v136
	s_waitcnt lgkmcnt(4)
	v_mfma_f32_16x16x32_bf16 v[66:69], v[200:203], v[114:117], v[66:69]
	v_exp_f32_e32 v242, v226
	v_mfma_f32_16x16x32_bf16 v[74:77], v[200:203], v[118:121], v[74:77]
	v_exp_f32_e32 v244, v227
	s_waitcnt lgkmcnt(2)
	v_mfma_f32_16x16x32_bf16 v[42:45], v[164:167], v[122:125], v[42:45]
	v_exp_f32_e32 v243, v148
	v_mfma_f32_16x16x32_bf16 v[46:49], v[164:167], v[126:129], v[46:49]
	v_exp_f32_e32 v245, v149
	s_waitcnt lgkmcnt(0)
	v_mfma_f32_16x16x32_bf16 v[66:69], v[204:207], v[122:125], v[66:69]
	v_exp_f32_e32 v142, v142
	v_mfma_f32_16x16x32_bf16 v[74:77], v[204:207], v[126:129], v[74:77]
	v_exp_f32_e32 v144, v144
	s_add_u32 s14, s14, 0x90000
	s_addc_u32 s15, s15, 0
	s_cmp_lg_u32 s14, 0x9120000
	s_mov_b32 s16, s17
	s_cbranch_scc1 .LBB0_650
	v_mov_b32_e32 v156, v240
	v_mov_b32_e32 v157, v241
	v_mov_b32_e32 v158, v246
	v_mov_b32_e32 v159, v247
	v_mov_b32_e32 v164, v242
	v_mov_b32_e32 v165, v243
	v_mov_b32_e32 v166, v244
	v_mov_b32_e32 v167, v245
	s_setprio 1
	s_waitcnt vmcnt(1)
	v_cvt_pk_bf16_f32 v106, v158, v152
	v_cvt_pk_bf16_f32 v107, v156, v160
	v_cvt_pk_bf16_f32 v108, v168, v170
	v_cvt_pk_bf16_f32 v109, v164, v166
	s_waitcnt vmcnt(0)
	v_cvt_pk_bf16_f32 v110, v159, v153
	v_cvt_pk_bf16_f32 v111, v157, v161
	v_cvt_pk_bf16_f32 v112, v169, v171
	v_cvt_pk_bf16_f32 v113, v165, v167
	v_cvt_pk_bf16_f32 v114, v142, v172
	v_cvt_pk_bf16_f32 v115, v144, v174
	v_cvt_pk_bf16_f32 v116, v134, v138
	v_cvt_pk_bf16_f32 v117, v136, v140
	v_cvt_pk_bf16_f32 v118, v143, v173
	v_cvt_pk_bf16_f32 v119, v145, v175
	v_cvt_pk_bf16_f32 v120, v135, v139
	v_cvt_pk_bf16_f32 v121, v137, v141
	s_waitcnt lgkmcnt(0)
	s_barrier
; #define SBAR() __builtin_amdgcn_sched_barrier(0)
; template <int LDQ, int LDK, int LDO>
; __device__ __forceinline__ void attn_gqa16_body(const bf16* __restrict__ Qb, const bf16* __restrict__ Kh, const bf16* __restrict__ Vh, bf16* __restrict__ Ob, int seq, char* lds, float mref) {
;     ...
;   for (int t = 0; t < NT; ++t) {
;     HPACK();
;     __syncthreads();
;     const bool more = t + 1 < NT;
;     if (more) HQK((t + 1) & 1);
;     const int vb = vb0 + (t & 1) * (int)G16_V;
;     SBAR(); pv16<0>(o, vb, pb); SBAR();
	s_mov_b32 m0, s86
	s_nop 0
	global_load_lds_dwordx4 v253, s[74:75]
	s_add_i32 m0, s86, 0x400
	s_nop 0
	global_load_lds_dwordx4 v253, s[76:77]
	ds_read_b128 v[122:125], v182 offset:50688
	ds_read_b128 v[126:129], v182 offset:50752
	ds_read_b128 v[146:149], v182 offset:55040
	ds_read_b128 v[196:199], v182 offset:55104
	ds_read_b128 v[204:207], v182 offset:59392
	ds_read_b128 v[208:211], v182 offset:59456
	ds_read_b128 v[216:219], v182 offset:63744
	ds_read_b128 v[220:223], v182 offset:63808
	s_waitcnt lgkmcnt(7)
	v_mfma_f32_16x16x32_bf16 v[130:133], v[122:125], v[30:33], 0
	v_mov_b32_e32 v190, v168
	v_mov_b32_e32 v191, v158
	v_mov_b32_e32 v192, v170
	v_mfma_f32_16x16x32_bf16 v[122:125], v[122:125], v[38:41], 0
	v_mov_b32_e32 v193, v152
	v_mov_b32_e32 v152, v171
	s_lshl_b32 s8, s8, 12
	s_waitcnt lgkmcnt(5)
	v_mfma_f32_16x16x32_bf16 v[200:203], v[146:149], v[30:33], 0
	s_add_u32 s8, s42, s8
	s_addc_u32 s14, s43, 0
	s_add_u32 s12, s8, s12
	v_mfma_f32_16x16x32_bf16 v[146:149], v[146:149], v[38:41], 0
	s_addc_u32 s13, s14, s13
	s_waitcnt lgkmcnt(3)
	v_mfma_f32_16x16x32_bf16 v[212:215], v[204:207], v[30:33], 0
	s_waitcnt lgkmcnt(1)
	v_mfma_f32_16x16x32_bf16 v[30:33], v[216:219], v[30:33], 0
	v_mfma_f32_16x16x32_bf16 v[130:133], v[126:129], v[18:21], v[130:133]
	v_mfma_f32_16x16x32_bf16 v[122:125], v[126:129], v[22:25], v[122:125]
	v_mfma_f32_16x16x32_bf16 v[126:129], v[196:199], v[18:21], v[200:203]
	v_mfma_f32_16x16x32_bf16 v[146:149], v[196:199], v[22:25], v[146:149]
	v_mfma_f32_16x16x32_bf16 v[196:199], v[208:211], v[18:21], v[212:215]
	s_waitcnt lgkmcnt(0)
	v_mfma_f32_16x16x32_bf16 v[18:21], v[220:223], v[18:21], v[30:33]
	s_nop 0
	v_mov_b32_e32 v213, v156
	v_mov_b32_e32 v212, v164
	v_mov_b32_e32 v214, v166
	ds_read_b128 v[30:33], v182 offset:50816
	v_mfma_f32_16x16x32_bf16 v[204:207], v[204:207], v[38:41], 0
	v_mov_b32_e32 v215, v160
	v_mfma_f32_16x16x32_bf16 v[38:41], v[216:219], v[38:41], 0
	v_mov_b32_e32 v216, v169
	v_mov_b32_e32 v217, v159
	v_mov_b32_e32 v219, v157
	v_mfma_f32_16x16x32_bf16 v[200:203], v[208:211], v[22:25], v[204:207]
	v_mov_b32_e32 v218, v165
	v_mfma_f32_16x16x32_bf16 v[22:25], v[220:223], v[22:25], v[38:41]
	s_nop 2
	ds_read_b128 v[38:41], v182 offset:55168
	ds_read_b128 v[204:207], v182 offset:50880
	s_waitcnt lgkmcnt(2)
	v_mfma_f32_16x16x32_bf16 v[130:133], v[30:33], v[10:13], v[130:133]
	v_mfma_f32_16x16x32_bf16 v[30:33], v[30:33], v[14:17], v[122:125]
	s_nop 2
	ds_read_b128 v[122:125], v182 offset:59520
	ds_read_b128 v[208:211], v182 offset:55232
	s_waitcnt lgkmcnt(3)
	v_mfma_f32_16x16x32_bf16 v[126:129], v[38:41], v[10:13], v[126:129]
	v_mfma_f32_16x16x32_bf16 v[38:41], v[38:41], v[14:17], v[146:149]
	s_nop 2
	ds_read_b128 v[146:149], v182 offset:63872
	ds_read_b128 v[168:171], v182 offset:59584
	ds_read_b128 v[156:159], v182 offset:63936
	s_waitcnt lgkmcnt(4)
	v_mfma_f32_16x16x32_bf16 v[196:199], v[122:125], v[10:13], v[196:199]
	s_waitcnt lgkmcnt(2)
	v_mfma_f32_16x16x32_bf16 v[10:13], v[146:149], v[10:13], v[18:21]
	v_mfma_f32_16x16x32_bf16 v[122:125], v[122:125], v[14:17], v[200:203]
	s_nop 1
	v_mov_b32_e32 v18, v142
	v_mov_b32_e32 v19, v144
	v_mov_b32_e32 v20, v172
	v_mfma_f32_16x16x32_bf16 v[14:17], v[146:149], v[14:17], v[22:25]
	v_mov_b32_e32 v201, v161
	v_mov_b32_e32 v200, v167
	v_mov_b32_e32 v21, v174
	v_mfma_f32_16x16x32_bf16 v[160:163], v[204:207], v[6:9], v[30:33]
	v_add_f32_e64 v24, v190, v192
	v_add_f32_e64 v25, v191, v193
	v_mov_b32_e32 v144, v143
	v_mov_b32_e32 v22, v173
	v_pk_add_f32 v[30:31], v[212:213], v[214:215]
	v_mfma_f32_16x16x32_bf16 v[146:149], v[204:207], v[2:5], v[130:133]
	v_add_f32_e64 v24, v24, v30
	v_add_f32_e64 v25, v25, v31
	v_mov_b32_e32 v23, v175
	v_pk_add_f32 v[32:33], v[216:217], v[152:153]
	v_mfma_f32_16x16x32_bf16 v[164:167], v[208:211], v[2:5], v[126:129]
	v_add_f32_e64 v144, v144, v22
	v_add_f32_e64 v145, v145, v23
	v_add_f32_e32 v130, v134, v138
	v_add_f32_e32 v132, v136, v140
	v_mfma_f32_16x16x32_bf16 v[172:175], v[208:211], v[6:9], v[38:41]
	v_add_f32_e64 v126, v18, v20
	v_add_f32_e64 v127, v19, v21
	s_nop 0
	v_pk_add_f32 v[38:39], v[218:219], v[200:201]
	s_waitcnt lgkmcnt(1)
	v_mfma_f32_16x16x32_bf16 v[196:199], v[168:171], v[2:5], v[196:199]
	v_add_f32_e64 v142, v32, v38
	v_add_f32_e64 v143, v33, v39
	s_waitcnt lgkmcnt(0)
	v_mfma_f32_16x16x32_bf16 v[200:203], v[156:159], v[2:5], v[10:13]
	v_add_f32_e64 v2, v150, v25
	v_add_f32_e64 v3, v151, v24
	v_pk_add_f32 v[128:129], v[24:25], v[2:3]
	v_mfma_f32_16x16x32_bf16 v[168:171], v[168:171], v[6:9], v[122:125]
	s_nop 2
	v_add_f32_e32 v122, v135, v139
	v_add_f32_e32 v124, v137, v141
	v_mfma_f32_16x16x32_bf16 v[134:137], v[156:159], v[6:9], v[14:17]
	ds_read_b64_tr_b16 v[2:3], v183 offset:0
	ds_read_b64_tr_b16 v[4:5], v183 offset:0x200
	ds_read_b64_tr_b16 v[6:7], v183 offset:0x400
	ds_read_b64_tr_b16 v[8:9], v183 offset:0x600
	ds_read_b64_tr_b16 v[10:11], v183 offset:0x820
	ds_read_b64_tr_b16 v[12:13], v183 offset:0xa20
	ds_read_b64_tr_b16 v[14:15], v183 offset:0xc20
	ds_read_b64_tr_b16 v[16:17], v183 offset:0xe20
	ds_read_b64_tr_b16 v[18:19], v183 offset:0x1040
	ds_read_b64_tr_b16 v[20:21], v183 offset:0x1240
	ds_read_b64_tr_b16 v[22:23], v183 offset:0x1440
	ds_read_b64_tr_b16 v[24:25], v183 offset:0x1640
	s_waitcnt lgkmcnt(4)
	s_nop 0
	v_mfma_f32_16x16x32_bf16 v[30:33], v[2:5], v[106:109], v[102:105]
	v_mfma_f32_16x16x32_bf16 v[38:41], v[2:5], v[110:113], v[98:101]
	v_mfma_f32_16x16x32_bf16 v[94:97], v[10:13], v[106:109], v[94:97]
	v_mfma_f32_16x16x32_bf16 v[10:13], v[10:13], v[110:113], v[90:93]
	v_mfma_f32_16x16x32_bf16 v[2:5], v[6:9], v[114:117], v[30:33]
	v_mfma_f32_16x16x32_bf16 v[6:9], v[6:9], v[118:121], v[38:41]
	v_mfma_f32_16x16x32_bf16 v[38:41], v[14:17], v[114:117], v[94:97]
	v_mfma_f32_16x16x32_bf16 v[90:93], v[14:17], v[118:121], v[10:13]
	ds_read_b64_tr_b16 v[14:15], v183 offset:0x1860
	ds_read_b64_tr_b16 v[16:17], v183 offset:0x1a60
	ds_read_b64_tr_b16 v[30:31], v183 offset:0x1c60
	ds_read_b64_tr_b16 v[32:33], v183 offset:0x1e60
	s_waitcnt lgkmcnt(4)
; #define SBAR() __builtin_amdgcn_sched_barrier(0)
; #define MFMA16(a, b, c) __builtin_amdgcn_mfma_f32_16x16x32_bf16(a, b, c, 0, 0, 0)
; template <int D0> __device__ __forceinline__ void pv16(f32x4a (&o)[8][2], int vb, const bf16x8 (&pb)[2][2]) {
;     ...
;   const s16x4 a0 = TR(D0, 0, 0), a1 = TR(D0, 0, 1), a2 = TR(D0, 1, 0), a3 = TR(D0, 1, 1), b0 = TR(D0 + 1, 0, 0), b1 = TR(D0 + 1, 0, 1), b2 = TR(D0 + 1, 1, 0), b3 = TR(D0 + 1, 1, 1);
;   const s16x4 c0 = TR(D0 + 2, 0, 0), c1 = TR(D0 + 2, 0, 1), c2 = TR(D0 + 2, 1, 0), c3 = TR(D0 + 2, 1, 1);
;   asm volatile("s_waitcnt lgkmcnt(4)" ::: "memory"); SBAR();
;   o[D0][0] = MFMA16(PK16(a0, a1), pb[0][0], o[D0][0]); o[D0][1] = MFMA16(PK16(a0, a1), pb[0][1], o[D0][1]);
;   o[D0 + 1][0] = MFMA16(PK16(b0, b1), pb[0][0], o[D0 + 1][0]); o[D0 + 1][1] = MFMA16(PK16(b0, b1), pb[0][1], o[D0 + 1][1]);
;   o[D0][0] = MFMA16(PK16(a2, a3), pb[1][0], o[D0][0]); o[D0][1] = MFMA16(PK16(a2, a3), pb[1][1], o[D0][1]);
;   o[D0 + 1][0] = MFMA16(PK16(b2, b3), pb[1][0], o[D0 + 1][0]); o[D0 + 1][1] = MFMA16(PK16(b2, b3), pb[1][1], o[D0 + 1][1]);
;   SBAR();
;   const s16x4 d0 = TR(D0 + 3, 0, 0), d1 = TR(D0 + 3, 0, 1), d2 = TR(D0 + 3, 1, 0), d3 = TR(D0 + 3, 1, 1);
;   asm volatile("s_waitcnt lgkmcnt(4)" ::: "memory"); SBAR();
;   o[D0 + 2][0] = MFMA16(PK16(c0, c1), pb[0][0], o[D0 + 2][0]); o[D0 + 2][1] = MFMA16(PK16(c0, c1), pb[0][1], o[D0 + 2][1]);
;   o[D0 + 2][0] = MFMA16(PK16(c2, c3), pb[1][0], o[D0 + 2][0]); o[D0 + 2][1] = MFMA16(PK16(c2, c3), pb[1][1], o[D0 + 2][1]);
;   asm volatile("s_waitcnt lgkmcnt(0)" ::: "memory"); SBAR();
;   o[D0 + 3][0] = MFMA16(PK16(d0, d1), pb[0][0], o[D0 + 3][0]); o[D0 + 3][1] = MFMA16(PK16(d0, d1), pb[0][1], o[D0 + 3][1]);
;   o[D0 + 3][0] = MFMA16(PK16(d2, d3), pb[1][0], o[D0 + 3][0]); o[D0 + 3][1] = MFMA16(PK16(d2, d3), pb[1][1], o[D0 + 3][1]);
	v_mfma_f32_16x16x32_bf16 v[10:13], v[18:21], v[106:109], v[78:81]
	s_waitcnt lgkmcnt(0)
	v_mfma_f32_16x16x32_bf16 v[18:21], v[18:21], v[110:113], v[50:53]
	v_mfma_f32_16x16x32_bf16 v[10:13], v[22:25], v[114:117], v[10:13]
	v_mfma_f32_16x16x32_bf16 v[22:25], v[22:25], v[118:121], v[18:21]
	v_mfma_f32_16x16x32_bf16 v[18:21], v[14:17], v[106:109], v[82:85]
	v_mfma_f32_16x16x32_bf16 v[50:53], v[14:17], v[110:113], v[86:89]
	v_mfma_f32_16x16x32_bf16 v[14:17], v[30:33], v[114:117], v[18:21]
	v_mfma_f32_16x16x32_bf16 v[18:21], v[30:33], v[118:121], v[50:53]
	s_waitcnt vmcnt(0)
	s_waitcnt vmcnt(1)
	s_waitcnt vmcnt(0)
	ds_read_b64_tr_b16 v[26:27], v183 offset:0x2080
	ds_read_b64_tr_b16 v[28:29], v183 offset:0x2280
	ds_read_b64_tr_b16 v[30:31], v183 offset:0x2480
	ds_read_b64_tr_b16 v[32:33], v183 offset:0x2680
	ds_read_b64_tr_b16 v[34:35], v183 offset:0x28a0
	ds_read_b64_tr_b16 v[36:37], v183 offset:0x2aa0
	ds_read_b64_tr_b16 v[78:79], v183 offset:0x2ca0
	ds_read_b64_tr_b16 v[80:81], v183 offset:0x2ea0
	ds_read_b64_tr_b16 v[82:83], v183 offset:0x30c0
	ds_read_b64_tr_b16 v[84:85], v183 offset:0x32c0
	ds_read_b64_tr_b16 v[86:87], v183 offset:0x34c0
	ds_read_b64_tr_b16 v[88:89], v183 offset:0x36c0
	s_waitcnt lgkmcnt(4)
	s_nop 0
	v_mfma_f32_16x16x32_bf16 v[50:53], v[26:29], v[106:109], v[54:57]
	v_mfma_f32_16x16x32_bf16 v[26:29], v[26:29], v[110:113], v[62:65]
	v_mfma_f32_16x16x32_bf16 v[58:61], v[34:37], v[106:109], v[58:61]
	v_mfma_f32_16x16x32_bf16 v[34:37], v[34:37], v[110:113], v[70:73]
	v_mfma_f32_16x16x32_bf16 v[50:53], v[30:33], v[114:117], v[50:53]
	v_mfma_f32_16x16x32_bf16 v[54:57], v[30:33], v[118:121], v[26:29]
	v_mfma_f32_16x16x32_bf16 v[70:73], v[78:81], v[114:117], v[58:61]
	v_mfma_f32_16x16x32_bf16 v[78:81], v[78:81], v[118:121], v[34:37]
	ds_read_b64_tr_b16 v[30:31], v183 offset:0x38e0
	ds_read_b64_tr_b16 v[32:33], v183 offset:0x3ae0
	ds_read_b64_tr_b16 v[34:35], v183 offset:0x3ce0
	ds_read_b64_tr_b16 v[36:37], v183 offset:0x3ee0
	s_waitcnt lgkmcnt(4)
	v_mfma_f32_16x16x32_bf16 v[26:29], v[82:85], v[106:109], v[42:45]
	s_waitcnt lgkmcnt(0)
	v_mfma_f32_16x16x32_bf16 v[42:45], v[82:85], v[110:113], v[46:49]
	v_mfma_f32_16x16x32_bf16 v[26:29], v[86:89], v[114:117], v[26:29]
	v_mfma_f32_16x16x32_bf16 v[58:61], v[86:89], v[118:121], v[42:45]
	v_mfma_f32_16x16x32_bf16 v[42:45], v[30:33], v[106:109], v[66:69]
	v_mfma_f32_16x16x32_bf16 v[46:49], v[30:33], v[110:113], v[74:77]
	v_mfma_f32_16x16x32_bf16 v[30:33], v[34:37], v[114:117], v[42:45]
	v_mfma_f32_16x16x32_bf16 v[62:65], v[34:37], v[118:121], v[46:49]
	s_nop 4
	v_add_f32_e32 v42, v186, v196
	v_exp_f32_e32 v116, v42
	v_add_f32_e32 v42, v186, v197
	v_exp_f32_e32 v117, v42
	v_add_f32_e32 v42, v186, v198
	v_exp_f32_e32 v118, v42
	v_add_f32_e32 v42, v186, v199
	v_exp_f32_e32 v119, v42
	v_add_f32_e32 v42, v186, v168
	v_add_f32_e32 v34, v186, v146
	v_exp_f32_e32 v98, v42
	v_add_f32_e32 v42, v186, v169
	v_exp_f32_e32 v131, v34
	v_add_f32_e32 v34, v186, v147
	v_exp_f32_e32 v99, v42
	v_add_f32_e32 v42, v186, v170
	v_exp_f32_e32 v133, v34
	v_add_f32_e32 v34, v186, v148
	v_exp_f32_e32 v100, v42
	v_add_f32_e32 v42, v186, v171
	v_exp_f32_e32 v74, v34
	v_add_f32_e32 v34, v186, v149
	v_exp_f32_e32 v101, v42
	v_add_f32_e32 v42, v186, v200
	v_exp_f32_e32 v129, v34
	v_add_f32_e32 v34, v186, v160
	v_exp_f32_e32 v120, v42
	v_add_f32_e32 v42, v186, v201
	v_exp_f32_e32 v123, v34
	v_add_f32_e32 v34, v186, v161
	v_exp_f32_e32 v121, v42
	v_add_f32_e32 v42, v186, v202
	v_exp_f32_e32 v125, v34
	v_add_f32_e32 v34, v186, v162
	v_exp_f32_e32 v75, v42
	v_add_f32_e32 v42, v186, v203
	v_exp_f32_e32 v76, v34
	v_add_f32_e32 v34, v186, v163
	v_exp_f32_e32 v77, v42
	v_add_f32_e32 v42, v186, v134
	v_exp_f32_e32 v87, v34
	v_add_f32_e32 v34, v186, v164
	v_exp_f32_e32 v102, v42
	v_add_f32_e32 v42, v186, v135
	v_exp_f32_e32 v66, v34
	v_add_f32_e32 v34, v186, v165
	v_exp_f32_e32 v103, v42
	v_add_f32_e32 v42, v186, v136
	v_exp_f32_e32 v68, v34
	v_add_f32_e32 v34, v186, v166
	v_exp_f32_e32 v43, v42
	v_exp_f32_e32 v67, v34
	v_add_f32_e32 v34, v186, v167
	v_add_f32_e32 v35, v186, v173
	v_exp_f32_e32 v69, v34
	v_add_f32_e32 v34, v186, v172
	v_exp_f32_e32 v36, v35
	v_add_f32_e32 v35, v186, v174
	v_add_f32_e32 v37, v186, v175
	v_add_f32_e32 v42, v186, v137
	v_exp_f32_e32 v34, v34
	v_exp_f32_e32 v35, v35
	v_exp_f32_e32 v37, v37
	v_exp_f32_e32 v45, v42
	v_add_f32_e32 v42, v143, v151
	v_pk_add_f32 v[48:49], v[144:145], v[144:145] op_sel:[0,1] op_sel_hi:[1,0]
	v_pk_add_f32 v[84:85], v[142:143], v[42:43] op_sel_hi:[1,0]
	v_mov_b32_e32 v49, v76
	v_mov_b32_e32 v85, v87
	v_pk_add_f32 v[46:47], v[122:123], v[124:125]
	v_pk_add_f32 v[48:49], v[48:49], v[84:85]
	v_add_f32_e32 v42, v98, v99
	v_pk_add_f32 v[46:47], v[46:47], v[48:49]
	v_pk_add_f32 v[48:49], v[34:35], v[36:37]
	v_pk_add_f32 v[46:47], v[46:47], v[46:47] op_sel:[0,1] op_sel_hi:[1,0]
	v_pk_add_f32 v[48:49], v[48:49], v[48:49] op_sel:[0,1] op_sel_hi:[1,0]
	v_add_f32_e32 v44, v100, v101
	v_mov_b32_e32 v47, v102
	v_mov_b32_e32 v49, v103
	v_pk_add_f32 v[46:47], v[46:47], v[48:49]
	v_pk_add_f32 v[48:49], v[42:43], v[44:45]
	v_cvt_pk_bf16_f32 v82, v131, v133
	v_cvt_pk_bf16_f32 v83, v74, v129
	v_cvt_pk_bf16_f32 v84, v66, v68
	v_cvt_pk_bf16_f32 v85, v67, v69
	v_cvt_pk_bf16_f32 v86, v123, v125
	s_nop 0
	v_pk_add_f32 v[46:47], v[46:47], v[48:49]
	v_pk_add_f32 v[48:49], v[126:127], v[126:127] op_sel:[0,1] op_sel_hi:[1,0]
	v_add_f32_e32 v122, v46, v47
	v_mov_b32_e32 v49, v74
	v_pk_add_f32 v[46:47], v[130:131], v[132:133]
	v_pk_add_f32 v[48:49], v[48:49], v[128:129]
	v_cvt_pk_bf16_f32 v87, v76, v87
	v_cvt_pk_bf16_f32 v88, v34, v36
	v_cvt_pk_bf16_f32 v89, v35, v37
	v_cvt_pk_bf16_f32 v94, v116, v117
	v_cvt_pk_bf16_f32 v95, v118, v119
	s_nop 0
	v_pk_add_f32 v[114:115], v[46:47], v[48:49]
	v_cvt_pk_bf16_f32 v96, v120, v121
	v_cvt_pk_bf16_f32 v97, v75, v77
	v_cvt_pk_bf16_f32 v98, v98, v99
	v_cvt_pk_bf16_f32 v99, v100, v101
	v_cvt_pk_bf16_f32 v100, v102, v103
	v_cvt_pk_bf16_f32 v101, v43, v45
	s_waitcnt lgkmcnt(0)
	s_barrier
; #define SBAR() __builtin_amdgcn_sched_barrier(0)
; #define MFMA16(a, b, c) __builtin_amdgcn_mfma_f32_16x16x32_bf16(a, b, c, 0, 0, 0)
; template <int D0> __device__ __forceinline__ void pv16(f32x4a (&o)[8][2], int vb, const bf16x8 (&pb)[2][2]) {
;     ...
;   const s16x4 a0 = TR(D0, 0, 0), a1 = TR(D0, 0, 1), a2 = TR(D0, 1, 0), a3 = TR(D0, 1, 1), b0 = TR(D0 + 1, 0, 0), b1 = TR(D0 + 1, 0, 1), b2 = TR(D0 + 1, 1, 0), b3 = TR(D0 + 1, 1, 1);
;   const s16x4 c0 = TR(D0 + 2, 0, 0), c1 = TR(D0 + 2, 0, 1), c2 = TR(D0 + 2, 1, 0), c3 = TR(D0 + 2, 1, 1);
;   asm volatile("s_waitcnt lgkmcnt(4)" ::: "memory"); SBAR();
;   o[D0][0] = MFMA16(PK16(a0, a1), pb[0][0], o[D0][0]); o[D0][1] = MFMA16(PK16(a0, a1), pb[0][1], o[D0][1]);
;   o[D0 + 1][0] = MFMA16(PK16(b0, b1), pb[0][0], o[D0 + 1][0]); o[D0 + 1][1] = MFMA16(PK16(b0, b1), pb[0][1], o[D0 + 1][1]);
;   o[D0][0] = MFMA16(PK16(a2, a3), pb[1][0], o[D0][0]); o[D0][1] = MFMA16(PK16(a2, a3), pb[1][1], o[D0][1]);
;   o[D0 + 1][0] = MFMA16(PK16(b2, b3), pb[1][0], o[D0 + 1][0]); o[D0 + 1][1] = MFMA16(PK16(b2, b3), pb[1][1], o[D0 + 1][1]);
;   SBAR();
;   const s16x4 d0 = TR(D0 + 3, 0, 0), d1 = TR(D0 + 3, 0, 1), d2 = TR(D0 + 3, 1, 0), d3 = TR(D0 + 3, 1, 1);
;   asm volatile("s_waitcnt lgkmcnt(4)" ::: "memory"); SBAR();
;   o[D0 + 2][0] = MFMA16(PK16(c0, c1), pb[0][0], o[D0 + 2][0]); o[D0 + 2][1] = MFMA16(PK16(c0, c1), pb[0][1], o[D0 + 2][1]);
;   o[D0 + 2][0] = MFMA16(PK16(c2, c3), pb[1][0], o[D0 + 2][0]); o[D0 + 2][1] = MFMA16(PK16(c2, c3), pb[1][1], o[D0 + 2][1]);
;   asm volatile("s_waitcnt lgkmcnt(0)" ::: "memory"); SBAR();
;   o[D0 + 3][0] = MFMA16(PK16(d0, d1), pb[0][0], o[D0 + 3][0]); o[D0 + 3][1] = MFMA16(PK16(d0, d1), pb[0][1], o[D0 + 3][1]);
;   o[D0 + 3][0] = MFMA16(PK16(d2, d3), pb[1][0], o[D0 + 3][0]); o[D0 + 3][1] = MFMA16(PK16(d2, d3), pb[1][1], o[D0 + 3][1]);
; template <int LDQ, int LDK, int LDO>
; __device__ __forceinline__ void attn_gqa16_body(const bf16* __restrict__ Qb, const bf16* __restrict__ Kh, const bf16* __restrict__ Vh, bf16* __restrict__ Ob, int seq, char* lds, float mref) {
;     ...
;   __builtin_amdgcn_s_setprio(0);
;   ls0 += __shfl_xor(ls0, 16); ls0 += __shfl_xor(ls0, 32); ls1 += __shfl_xor(ls1, 16); ls1 += __shfl_xor(ls1, 32);
;   const float rl[2] = {__builtin_amdgcn_rcpf(ls0), __builtin_amdgcn_rcpf(ls1)};
	ds_read_b64_tr_b16 v[34:35], v184 offset:0
	ds_read_b64_tr_b16 v[36:37], v184 offset:0x200
	ds_read_b64_tr_b16 v[42:43], v184 offset:0x400
	ds_read_b64_tr_b16 v[44:45], v184 offset:0x600
	ds_read_b64_tr_b16 v[46:47], v184 offset:0x820
	ds_read_b64_tr_b16 v[48:49], v184 offset:0xa20
	ds_read_b64_tr_b16 v[102:103], v184 offset:0xc20
	ds_read_b64_tr_b16 v[104:105], v184 offset:0xe20
	ds_read_b64_tr_b16 v[106:107], v184 offset:0x1040
	ds_read_b64_tr_b16 v[108:109], v184 offset:0x1240
	ds_read_b64_tr_b16 v[110:111], v184 offset:0x1440
	ds_read_b64_tr_b16 v[112:113], v184 offset:0x1640
	s_waitcnt lgkmcnt(4)
	s_nop 0
	v_mfma_f32_16x16x32_bf16 v[2:5], v[34:37], v[82:85], v[2:5]
	v_mfma_f32_16x16x32_bf16 v[6:9], v[34:37], v[86:89], v[6:9]
	v_mfma_f32_16x16x32_bf16 v[34:37], v[46:49], v[82:85], v[38:41]
	v_mfma_f32_16x16x32_bf16 v[46:49], v[46:49], v[86:89], v[90:93]
	v_mfma_f32_16x16x32_bf16 v[38:41], v[42:45], v[94:97], v[2:5]
	v_mfma_f32_16x16x32_bf16 v[6:9], v[42:45], v[98:101], v[6:9]
	v_mfma_f32_16x16x32_bf16 v[34:37], v[102:105], v[94:97], v[34:37]
	v_mfma_f32_16x16x32_bf16 v[2:5], v[102:105], v[98:101], v[46:49]
	ds_read_b64_tr_b16 v[46:47], v184 offset:0x1860
	ds_read_b64_tr_b16 v[48:49], v184 offset:0x1a60
	ds_read_b64_tr_b16 v[90:91], v184 offset:0x1c60
	ds_read_b64_tr_b16 v[92:93], v184 offset:0x1e60
	s_waitcnt lgkmcnt(4)
	v_mfma_f32_16x16x32_bf16 v[10:13], v[106:109], v[82:85], v[10:13]
	s_waitcnt lgkmcnt(0)
	v_mfma_f32_16x16x32_bf16 v[22:25], v[106:109], v[86:89], v[22:25]
	v_mfma_f32_16x16x32_bf16 v[42:45], v[110:113], v[94:97], v[10:13]
	v_mfma_f32_16x16x32_bf16 v[10:13], v[110:113], v[98:101], v[22:25]
	v_mfma_f32_16x16x32_bf16 v[14:17], v[46:49], v[82:85], v[14:17]
	v_mfma_f32_16x16x32_bf16 v[18:21], v[46:49], v[86:89], v[18:21]
	v_mfma_f32_16x16x32_bf16 v[46:49], v[90:93], v[94:97], v[14:17]
	v_mfma_f32_16x16x32_bf16 v[14:17], v[90:93], v[98:101], v[18:21]
	s_waitcnt vmcnt(0)
	ds_read_b64_tr_b16 v[18:19], v184 offset:0x2080
	ds_read_b64_tr_b16 v[20:21], v184 offset:0x2280
	ds_read_b64_tr_b16 v[22:23], v184 offset:0x2480
	ds_read_b64_tr_b16 v[24:25], v184 offset:0x2680
	ds_read_b64_tr_b16 v[90:91], v184 offset:0x28a0
	ds_read_b64_tr_b16 v[92:93], v184 offset:0x2aa0
	ds_read_b64_tr_b16 v[102:103], v184 offset:0x2ca0
	ds_read_b64_tr_b16 v[104:105], v184 offset:0x2ea0
	ds_read_b64_tr_b16 v[106:107], v184 offset:0x30c0
	ds_read_b64_tr_b16 v[108:109], v184 offset:0x32c0
	ds_read_b64_tr_b16 v[110:111], v184 offset:0x34c0
	ds_read_b64_tr_b16 v[112:113], v184 offset:0x36c0
	s_waitcnt lgkmcnt(4)
	s_nop 5
	v_mfma_f32_16x16x32_bf16 v[50:53], v[18:21], v[82:85], v[50:53]
	v_mfma_f32_16x16x32_bf16 v[18:21], v[18:21], v[86:89], v[54:57]
	v_mfma_f32_16x16x32_bf16 v[70:73], v[90:93], v[82:85], v[70:73]
	v_mfma_f32_16x16x32_bf16 v[78:81], v[90:93], v[86:89], v[78:81]
	v_mfma_f32_16x16x32_bf16 v[54:57], v[22:25], v[94:97], v[50:53]
	v_mfma_f32_16x16x32_bf16 v[22:25], v[22:25], v[98:101], v[18:21]
	v_mfma_f32_16x16x32_bf16 v[50:53], v[102:105], v[94:97], v[70:73]
	v_mfma_f32_16x16x32_bf16 v[18:21], v[102:105], v[98:101], v[78:81]
	ds_read_b64_tr_b16 v[70:71], v184 offset:0x38e0
	ds_read_b64_tr_b16 v[72:73], v184 offset:0x3ae0
	ds_read_b64_tr_b16 v[78:79], v184 offset:0x3ce0
	ds_read_b64_tr_b16 v[80:81], v184 offset:0x3ee0
	s_waitcnt lgkmcnt(4)
	v_mfma_f32_16x16x32_bf16 v[26:29], v[106:109], v[82:85], v[26:29]
	s_waitcnt lgkmcnt(0)
	v_mfma_f32_16x16x32_bf16 v[90:93], v[106:109], v[86:89], v[58:61]
	v_mfma_f32_16x16x32_bf16 v[58:61], v[110:113], v[94:97], v[26:29]
	v_mfma_f32_16x16x32_bf16 v[26:29], v[110:113], v[98:101], v[90:93]
	v_mfma_f32_16x16x32_bf16 v[30:33], v[70:73], v[82:85], v[30:33]
	v_mfma_f32_16x16x32_bf16 v[70:73], v[70:73], v[86:89], v[62:65]
	v_mfma_f32_16x16x32_bf16 v[62:65], v[78:81], v[94:97], v[30:33]
	v_mfma_f32_16x16x32_bf16 v[30:33], v[78:81], v[98:101], v[70:73]
	v_add_f32_e64 v66, v66, v68
	v_add_f32_e64 v67, v67, v69
	v_pk_add_f32 v[68:69], v[114:115], v[114:115] op_sel:[0,1] op_sel_hi:[1,0]
	v_pk_add_f32 v[66:67], v[66:67], v[66:67] op_sel:[0,1] op_sel_hi:[1,0]
	v_add_f32_e32 v74, v116, v117
	v_add_f32_e32 v76, v118, v119
	v_mov_b32_e32 v69, v120
	v_mov_b32_e32 v67, v121
	v_pk_add_f32 v[66:67], v[68:69], v[66:67]
	v_pk_add_f32 v[68:69], v[74:75], v[76:77]
	s_nop 0
	v_pk_add_f32 v[66:67], v[66:67], v[68:69]
	s_nop 0
	v_add_f32_e32 v66, v66, v67
	s_setprio 0
	ds_bpermute_b32 v67, v177, v66
	ds_bpermute_b32 v68, v177, v122
	v_mov_b32_e32 v70, v185
	s_waitcnt lgkmcnt(1)
	v_add_f32_e32 v66, v66, v67
	s_waitcnt lgkmcnt(0)
	v_add_f32_e32 v67, v122, v68
	ds_bpermute_b32 v68, v188, v66
	ds_bpermute_b32 v69, v188, v67
	s_waitcnt lgkmcnt(1)
	v_add_f32_e32 v66, v66, v68
	s_waitcnt lgkmcnt(0)
	v_add_f32_e32 v67, v67, v69
	v_rcp_f32_e32 v68, v66
	v_rcp_f32_e32 v66, v67
	v_mov_b32_e32 v67, v176
	v_mov_b32_e32 v69, v180
	s_branch .LBB0_641

; __device__ __forceinline__ unsigned xb_ld(unsigned* p)              { return __hip_atomic_load(p, __ATOMIC_RELAXED, __HIP_MEMORY_SCOPE_AGENT); }
; __device__ __forceinline__ unsigned xb_add(unsigned* p, unsigned v) { return __hip_atomic_fetch_add(p, v, __ATOMIC_RELAXED, __HIP_MEMORY_SCOPE_AGENT); }
; __device__ __forceinline__ void xcd_barrier_complete(unsigned* bar, unsigned x, unsigned& nloc, unsigned& nx) {
;     const unsigned G = gridDim.x * gridDim.y * gridDim.z;
;     unsigned sum, cnt, mine, sp = 0u;
;     for (;;) {
;         sum = 0u; cnt = 0u; mine = 0u;
; #pragma unroll
;         for (unsigned j = 0; j < 16; ++j) { const unsigned c = xb_ld(&bar[XB_XCNT(j)]); sum += c; cnt += (c > 0u) ? 1u : 0u; mine = (j == x) ? c : mine; }
; __device__ __forceinline__ void xcd_barrier(const XcdBarrier& b) {
;     asm volatile("s_waitcnt vmcnt(0)" ::: "memory");
;     __syncthreads();
;     if (threadIdx.x == 0) {
;         unsigned* bar = b.bar;
;         __builtin_amdgcn_s_waitcnt(0);
;         unsigned nloc = b.st[0], nx = b.st[1];
;         if (nloc == 0u) { xcd_barrier_complete(bar, b.x, nloc, nx); b.st[0] = nloc; b.st[1] = nx; }
;         const unsigned old = xb_add(&bar[XB_XSUB(b.x)], 1u);
;         const unsigned gen = old / nloc;
;         if (old + 1u == (gen + 1u) * nloc) {
.LBB0_653:
	s_nop 0
	s_nop 0
	s_nop 0
	s_nop 0
	s_nop 0
	s_nop 0
	s_nop 0
	s_nop 0
	s_nop 0
	s_nop 0
	s_nop 0
	s_nop 0
	s_cmp_gt_i32 s81, 8
	s_cselect_b64 s[4:5], -1, 0
	s_and_b64 s[0:1], s[10:11], s[4:5]
	s_andn2_b64 vcc, exec, s[0:1]
	s_cbranch_vccnz .LBB0_707
	s_mov_b64 s[8:9], s[96:97]
	s_getreg_b32 s0, hwreg(HW_REG_XCC_ID, 0, 4)
	s_waitcnt vmcnt(0)
	s_waitcnt vmcnt(0)
	s_barrier
	s_mov_b64 s[6:7], exec
	v_readlane_b32 s2, v255, 0
	v_readlane_b32 s3, v255, 1
	s_and_b64 s[2:3], s[6:7], s[2:3]
	s_mov_b64 exec, s[2:3]
	s_cbranch_execz .LBB0_706
	s_add_i32 s1, 0, 0x22160
	v_mov_b32_e32 v2, s1
	s_load_dwordx2 s[8:9], s[8:9], 0xe8
	s_waitcnt vmcnt(0) expcnt(0) lgkmcnt(0)
	ds_read_b32 v4, v2
	s_add_i32 s1, 0, 0x22164
	v_mov_b32_e32 v2, s1
	ds_read_b32 v2, v2
	s_and_b32 s0, s0, 15
	s_waitcnt lgkmcnt(1)
	v_cmp_ne_u32_e32 vcc, 0, v4
	s_cbranch_vccnz .LBB0_670
	s_add_u32 s10, s8, 0x4200
	s_addc_u32 s11, s9, 0
	s_add_u32 s12, s8, 0x4400
	s_addc_u32 s13, s9, 0
	s_add_u32 s14, s8, 0x4500
	s_addc_u32 s15, s9, 0
	s_add_u32 s16, s8, 0x4600
	s_addc_u32 s17, s9, 0
	s_add_u32 s18, s8, 0x4700
	s_addc_u32 s19, s9, 0
	s_add_u32 s20, s8, 0x4800
	s_addc_u32 s21, s9, 0
	s_add_u32 s22, s8, 0x4900
	s_addc_u32 s23, s9, 0
	s_add_u32 s24, s8, 0x4a00
	s_addc_u32 s25, s9, 0
	s_add_u32 s26, s8, 0x4b00
	s_addc_u32 s27, s9, 0
	s_add_u32 s28, s8, 0x4c00
	s_addc_u32 s29, s9, 0
	s_add_u32 s30, s8, 0x4d00
	s_addc_u32 s31, s9, 0
	s_add_u32 s34, s8, 0x4e00
	s_addc_u32 s35, s9, 0
	s_add_u32 s36, s8, 0x4f00
	s_addc_u32 s37, s9, 0
	s_add_u32 s38, s8, 0x5000
	s_addc_u32 s39, s9, 0
	s_load_dwordx2 s[2:3], s[96:97], 0xf8
	s_load_dword s1, s[96:97], 0x100
	s_add_u32 s40, s8, 0x5100
	s_addc_u32 s41, s9, 0
	s_add_u32 s42, s8, 0x5200
	s_addc_u32 s43, s9, 0
	s_waitcnt lgkmcnt(0)
	s_mul_i32 s2, s3, s2
	s_add_u32 s44, s8, 0x5300
	s_mul_i32 s1, s2, s1
	s_addc_u32 s45, s9, 0
	s_mov_b32 s2, 1
	v_mov_b32_e32 v18, 0
	s_branch .LBB0_658
